# pooling mixer rewritten by hand (U rows register-prefetched two units ahead, LDS reads batched, W fragments and pool_scale in registers, dwordx2 stores) + P0 mod item 4-round prefetch with rcp sigmoid
# speedup vs baseline: 1.0446x; 1.0446x over previous
.LBB0_8:
	s_lshr_b32 s97, s3, 6
	s_lshl_b32 s0, s78, 3
	s_add_i32 s33, s0, s97
	s_lshl_b32 s96, s72, 3
	v_writelane_b32 v255, s52, 5
	s_cmp_lt_i32 s46, 1
	s_cselect_b64 s[0:1], -1, 0
	v_writelane_b32 v255, s53, 6
	s_cmp_gt_i32 s47, 0
	v_writelane_b32 v255, s44, 7
	s_cselect_b64 s[4:5], -1, 0
	s_and_b64 s[10:11], s[0:1], s[4:5]
	v_writelane_b32 v255, s45, 8
	v_writelane_b32 v255, s46, 9
	s_andn2_b64 vcc, exec, s[10:11]
	v_writelane_b32 v255, s47, 10
	s_cbranch_vccnz .LBB0_46
	s_mov_b64 s[8:9], s[52:53]
	v_mov_b32_e32 v2, v0
	s_mov_b32 s101, s33
	s_cmpk_lg_i32 s72, 0x100
	s_cbranch_scc1 .Lp0_map_done
	s_cmpk_gt_u32 s78, 0xbf
	s_cbranch_scc1 .Lp0_map_hi
	s_lshl_b32 s101, s78, 2
	s_and_b32 s100, s97, 3
	s_add_i32 s101, s101, s100
	s_cmp_lt_u32 s97, 4
	s_cbranch_scc1 .Lp0_map_done
	s_addk_i32 s101, 0x300
	s_branch .Lp0_map_done
.Lp0_map_hi:
	s_sub_i32 s101, s78, 0xc0
	s_lshl_b32 s101, s101, 3
	s_add_i32 s101, s101, s97
	s_addk_i32 s101, 0x600
.Lp0_map_done:
	s_cmpk_gt_i32 s101, 0x6af
	s_cbranch_scc1 .LBB0_46
	v_lshlrev_b32_e32 v3, 2, v2
	v_and_b32_e32 v4, 60, v3
	v_lshlrev_b32_e32 v3, 1, v2
	v_and_b32_e32 v156, 0x60, v3
	v_and_b32_e32 v3, 7, v2
	s_mul_i32 s0, s97, 0x2400
	v_lshlrev_b32_e32 v6, 4, v3
	v_lshlrev_b32_e32 v8, 3, v3
	v_lshlrev_b32_e32 v3, 4, v2
	s_load_dwordx2 s[28:29], s[8:9], 0xd8
	s_load_dwordx4 s[4:7], s[8:9], 0x8
	s_load_dwordx4 s[12:15], s[8:9], 0x20
	s_load_dwordx2 s[20:21], s[8:9], 0x60
	s_load_dwordx2 s[22:23], s[8:9], 0x78
	s_load_dwordx2 s[24:25], s[8:9], 0xb0
	s_load_dwordx4 s[16:19], s[8:9], 0xa0
	s_add_i32 s8, s0, 0
	v_mov_b32_e32 v135, 0
	v_and_b32_e32 v134, 0x70, v3
	v_add_u32_e32 v5, s8, v156
	v_add_u32_e32 v12, s8, v6
	v_add_u32_e32 v166, s8, v134
	s_waitcnt lgkmcnt(0)
	v_lshl_add_u64 v[10:11], s[28:29], 0, v[134:135]
	s_mov_b64 s[8:9], 0xc80000
	v_lshl_add_u64 v[136:137], v[10:11], 0, s[8:9]
	s_mov_b64 s[8:9], 0xb80000
	v_mov_b32_e32 v7, v135
	s_add_u32 s0, s28, 0xd00000
	v_lshl_add_u64 v[138:139], v[10:11], 0, s[8:9]
	v_lshl_add_u64 v[6:7], s[28:29], 0, v[6:7]
	s_mov_b64 s[8:9], 0xb00000
	s_addc_u32 s1, s29, 0
	v_lshl_add_u64 v[140:141], v[6:7], 0, s[8:9]
	v_bfe_u32 v7, v2, 5, 1
	s_bfe_u32 s26, s3, 0x20006
	v_and_b32_e32 v1, 48, v2
	v_bfe_u32 v157, v2, 3, 3
	v_and_b32_e32 v6, 31, v2
	v_lshl_or_b32 v2, s26, 8, v7
	v_mul_u32_u24_e32 v13, 0x1800, v2
	v_lshl_or_b32 v2, s26, 5, v6
	v_mul_u32_u24_e32 v2, 0x1800, v2
	s_mov_b64 s[8:9], 0x900000
	v_lshlrev_b32_e32 v134, 2, v2
	v_lshl_add_u64 v[142:143], v[10:11], 0, s[8:9]
	s_mov_b64 s[8:9], 0x500000
	v_lshl_add_u64 v[2:3], s[28:29], 0, v[134:135]
	v_lshlrev_b32_e32 v134, 4, v7
	v_lshl_add_u64 v[144:145], v[10:11], 0, s[8:9]
	v_lshl_add_u64 v[2:3], v[2:3], 0, v[134:135]
	s_mov_b64 s[8:9], 0x100000
	v_lshl_add_u64 v[146:147], v[2:3], 0, s[8:9]
	v_lshlrev_b32_e32 v2, 2, v13
	v_lshl_or_b32 v134, v6, 2, v2
	v_lshl_add_u64 v[148:149], s[6:7], 0, v[134:135]
	s_lshl_b32 s6, s78, 6
	s_lshl_b32 s7, s97, 3
	v_lshlrev_b32_e32 v10, 12, v6
	v_lshlrev_b32_e32 v11, 2, v7
	s_lshl_b32 s30, s101, 3
	s_lshl_b32 s6, s26, 10
	v_or3_b32 v134, v10, s6, v11
	v_mul_u32_u24_e32 v9, 0x90, v4
	v_mul_u32_u24_e32 v158, 0x90, v157
	v_lshl_add_u64 v[2:3], s[4:5], 0, v[134:135]
	s_mov_b32 s27, 0
	v_or_b32_e32 v159, 8, v157
	v_or_b32_e32 v160, 16, v157
	v_or_b32_e32 v161, 24, v157
	v_or_b32_e32 v162, 32, v157
	v_or_b32_e32 v163, 40, v157
	v_or_b32_e32 v164, 48, v157
	v_or_b32_e32 v165, 56, v157
	s_mov_b32 s68, s78
	s_lshl_b32 s31, s72, 6
	v_lshl_add_u64 v[150:151], v[2:3], 0, 56
	s_movk_i32 s34, 0x1000
	v_add_u32_e32 v167, v5, v9
	v_lshlrev_b32_e32 v152, 1, v8
	v_add_u32_e32 v168, v12, v158
	s_movk_i32 s35, 0x2000
	s_movk_i32 s36, 0x3000
	s_movk_i32 s37, 0x4000
	s_movk_i32 s38, 0x5000
	s_movk_i32 s39, 0x6000
	s_movk_i32 s40, 0x7000
	s_mov_b32 s41, 0x8000
	s_mov_b32 s42, 0xa000
	s_mov_b32 s43, 0xc000
	s_mov_b32 s44, 0xe000
	s_mov_b32 s45, 0x10000
	s_mov_b32 s46, 0x12000
	s_mov_b32 s47, 0x14000
	s_mov_b32 s48, 0x16000
	s_mov_b32 s49, 0x18000
	s_mov_b32 s50, 0x1a000
	s_mov_b32 s51, 0x1c000
	s_mov_b32 s52, 0x1e000
	s_mov_b32 s53, 0x1f000
	s_mov_b32 s54, 0xc3e00000
	s_mov_b32 s55, 0x20000
	s_mov_b32 s56, 0x22000
	s_mov_b32 s57, 0x24000
	s_mov_b32 s58, 0x26000
	s_mov_b32 s59, 0x28000
	s_mov_b32 s60, 0x2a000
	s_mov_b32 s61, 0x2c000
	s_mov_b32 s62, 0x2e000
	s_mov_b32 s63, 0x30000
	s_mov_b32 s64, 0x32000
	s_mov_b32 s65, 0x34000
	s_mov_b32 s66, 0x36000
	s_mov_b32 s67, 0x38000
	s_mov_b32 s73, 0x3a000
	s_mov_b32 s75, 0x3c000
	s_mov_b32 s76, 0x3e000
	s_mov_b32 s77, 0x48000
	s_mov_b32 s79, 0x54000
	v_lshlrev_b32_e32 v154, 2, v4
	v_mov_b32_e32 v169, 0x43e00000
	s_mov_b32 s80, s101
	s_branch .LBB0_12

.Lmod_loop:
	s_waitcnt vmcnt(0)
	global_load_dwordx4 v[84:87], v[22:23], off offset:200
	global_load_dword v214, v20, s[98:99]
	s_add_u32 s98, s98, 0x6000
	s_addc_u32 s99, s99, 0
	global_load_dword v215, v20, s[98:99]
	s_add_u32 s98, s98, 0x6000
	s_addc_u32 s99, s99, 0
	global_load_dword v216, v20, s[98:99]
	s_add_u32 s98, s98, 0x6000
	s_addc_u32 s99, s99, 0
	global_load_dword v217, v20, s[98:99]
	s_add_u32 s98, s98, 0x1e000
	s_addc_u32 s99, s99, 0
	global_load_dwordx4 v[88:91], v[22:23], off offset:232
	global_load_dword v218, v20, s[98:99]
	s_add_u32 s98, s98, 0x6000
	s_addc_u32 s99, s99, 0
	global_load_dword v219, v20, s[98:99]
	s_add_u32 s98, s98, 0x6000
	s_addc_u32 s99, s99, 0
	global_load_dword v220, v20, s[98:99]
	s_add_u32 s98, s98, 0x6000
	s_addc_u32 s99, s99, 0
	global_load_dword v221, v20, s[98:99]
	s_add_u32 s98, s98, 0x1e000
	s_addc_u32 s99, s99, 0
	global_load_dwordx4 v[92:95], v[22:23], off offset:264
	global_load_dword v222, v20, s[98:99]
	s_add_u32 s98, s98, 0x6000
	s_addc_u32 s99, s99, 0
	global_load_dword v223, v20, s[98:99]
	s_add_u32 s98, s98, 0x6000
	s_addc_u32 s99, s99, 0
	global_load_dword v224, v20, s[98:99]
	s_add_u32 s98, s98, 0x6000
	s_addc_u32 s99, s99, 0
	global_load_dword v225, v20, s[98:99]
	s_add_u32 s98, s98, 0x1e000
	s_addc_u32 s99, s99, 0
	global_load_dwordx4 v[96:99], v[22:23], off offset:296
	global_load_dword v226, v20, s[98:99]
	s_add_u32 s98, s98, 0x6000
	s_addc_u32 s99, s99, 0
	global_load_dword v227, v20, s[98:99]
	s_add_u32 s98, s98, 0x6000
	s_addc_u32 s99, s99, 0
	global_load_dword v228, v20, s[98:99]
	s_add_u32 s98, s98, 0x6000
	s_addc_u32 s99, s99, 0
	global_load_dword v229, v20, s[98:99]
	s_add_u32 s98, s98, 0x1e000
	s_addc_u32 s99, s99, 0
	global_load_dwordx4 v[100:103], v[22:23], off offset:328
	global_load_dword v230, v20, s[98:99]
	s_add_u32 s98, s98, 0x6000
	s_addc_u32 s99, s99, 0
	global_load_dword v231, v20, s[98:99]
	s_add_u32 s98, s98, 0x6000
	s_addc_u32 s99, s99, 0
	global_load_dword v232, v20, s[98:99]
	s_add_u32 s98, s98, 0x6000
	s_addc_u32 s99, s99, 0
	global_load_dword v233, v20, s[98:99]
	s_add_u32 s98, s98, 0x1e000
	s_addc_u32 s99, s99, 0
	global_load_dwordx4 v[104:107], v[22:23], off offset:360
	global_load_dword v234, v20, s[98:99]
	s_add_u32 s98, s98, 0x6000
	s_addc_u32 s99, s99, 0
	global_load_dword v235, v20, s[98:99]
	s_add_u32 s98, s98, 0x6000
	s_addc_u32 s99, s99, 0
	global_load_dword v236, v20, s[98:99]
	s_add_u32 s98, s98, 0x6000
	s_addc_u32 s99, s99, 0
	global_load_dword v237, v20, s[98:99]
	s_add_u32 s98, s98, 0x1e000
	s_addc_u32 s99, s99, 0
	global_load_dwordx4 v[108:111], v[22:23], off offset:392
	global_load_dword v238, v20, s[98:99]
	s_add_u32 s98, s98, 0x6000
	s_addc_u32 s99, s99, 0
	global_load_dword v239, v20, s[98:99]
	s_add_u32 s98, s98, 0x6000
	s_addc_u32 s99, s99, 0
	global_load_dword v240, v20, s[98:99]
	s_add_u32 s98, s98, 0x6000
	s_addc_u32 s99, s99, 0
	global_load_dword v241, v20, s[98:99]
	s_add_u32 s98, s98, 0x1e000
	s_addc_u32 s99, s99, 0
	global_load_dwordx4 v[112:115], v[22:23], off offset:424
	global_load_dword v242, v20, s[98:99]
	s_add_u32 s98, s98, 0x6000
	s_addc_u32 s99, s99, 0
	global_load_dword v243, v20, s[98:99]
	s_add_u32 s98, s98, 0x6000
	s_addc_u32 s99, s99, 0
	global_load_dword v244, v20, s[98:99]
	s_add_u32 s98, s98, 0x6000
	s_addc_u32 s99, s99, 0
	global_load_dword v245, v20, s[98:99]
	s_add_u32 s98, s98, 0x1e000
	s_addc_u32 s99, s99, 0
	v_mul_f32_e32 v24, 0xbfb8aa3b, v52
	v_mul_f32_e32 v30, 0xbfb8aa3b, v53
	v_mul_f32_e32 v36, 0xbfb8aa3b, v54
	v_mul_f32_e32 v42, 0xbfb8aa3b, v55
	v_exp_f32_e32 v24, v24
	v_exp_f32_e32 v30, v30
	v_exp_f32_e32 v36, v36
	v_exp_f32_e32 v42, v42
	v_add_f32_e32 v24, 1.0, v24
	v_add_f32_e32 v30, 1.0, v30
	v_add_f32_e32 v36, 1.0, v36
	v_add_f32_e32 v42, 1.0, v42
	v_rcp_f32_e32 v24, v24
	v_rcp_f32_e32 v30, v30
	v_rcp_f32_e32 v36, v36
	v_rcp_f32_e32 v42, v42
	v_mul_f32_e32 v116, v52, v24
	v_mul_f32_e32 v117, v53, v30
	v_mul_f32_e32 v118, v54, v36
	v_mul_f32_e32 v119, v55, v42
	v_mul_f32_e32 v24, 0xbfb8aa3b, v56
	v_mul_f32_e32 v30, 0xbfb8aa3b, v57
	v_mfma_f32_32x32x2_f32 v[2:17], v182, v116, v[2:17]
	v_mul_f32_e32 v36, 0xbfb8aa3b, v58
	v_mul_f32_e32 v42, 0xbfb8aa3b, v59
	v_exp_f32_e32 v24, v24
	v_exp_f32_e32 v30, v30
	v_mfma_f32_32x32x2_f32 v[2:17], v183, v117, v[2:17]
	v_exp_f32_e32 v36, v36
	v_exp_f32_e32 v42, v42
	v_add_f32_e32 v24, 1.0, v24
	v_add_f32_e32 v30, 1.0, v30
	v_mfma_f32_32x32x2_f32 v[2:17], v184, v118, v[2:17]
	v_add_f32_e32 v36, 1.0, v36
	v_add_f32_e32 v42, 1.0, v42
	v_rcp_f32_e32 v24, v24
	v_rcp_f32_e32 v30, v30
	v_mfma_f32_32x32x2_f32 v[2:17], v185, v119, v[2:17]
	v_rcp_f32_e32 v36, v36
	v_rcp_f32_e32 v42, v42
	v_mul_f32_e32 v120, v56, v24
	v_mul_f32_e32 v121, v57, v30
	v_mul_f32_e32 v122, v58, v36
	v_mul_f32_e32 v123, v59, v42
	v_mul_f32_e32 v24, 0xbfb8aa3b, v60
	v_mul_f32_e32 v30, 0xbfb8aa3b, v61
	v_mfma_f32_32x32x2_f32 v[2:17], v186, v120, v[2:17]
	v_mul_f32_e32 v36, 0xbfb8aa3b, v62
	v_mul_f32_e32 v42, 0xbfb8aa3b, v63
	v_exp_f32_e32 v24, v24
	v_exp_f32_e32 v30, v30
	v_mfma_f32_32x32x2_f32 v[2:17], v187, v121, v[2:17]
	v_exp_f32_e32 v36, v36
	v_exp_f32_e32 v42, v42
	v_add_f32_e32 v24, 1.0, v24
	v_add_f32_e32 v30, 1.0, v30
	v_mfma_f32_32x32x2_f32 v[2:17], v188, v122, v[2:17]
	v_add_f32_e32 v36, 1.0, v36
	v_add_f32_e32 v42, 1.0, v42
	v_rcp_f32_e32 v24, v24
	v_rcp_f32_e32 v30, v30
	v_mfma_f32_32x32x2_f32 v[2:17], v189, v123, v[2:17]
	v_rcp_f32_e32 v36, v36
	v_rcp_f32_e32 v42, v42
	v_mul_f32_e32 v116, v60, v24
	v_mul_f32_e32 v117, v61, v30
	v_mul_f32_e32 v118, v62, v36
	v_mul_f32_e32 v119, v63, v42
	v_mul_f32_e32 v24, 0xbfb8aa3b, v64
	v_mul_f32_e32 v30, 0xbfb8aa3b, v65
	v_mfma_f32_32x32x2_f32 v[2:17], v190, v116, v[2:17]
	v_mul_f32_e32 v36, 0xbfb8aa3b, v66
	v_mul_f32_e32 v42, 0xbfb8aa3b, v67
	v_exp_f32_e32 v24, v24
	v_exp_f32_e32 v30, v30
	v_mfma_f32_32x32x2_f32 v[2:17], v191, v117, v[2:17]
	v_exp_f32_e32 v36, v36
	v_exp_f32_e32 v42, v42
	v_add_f32_e32 v24, 1.0, v24
	v_add_f32_e32 v30, 1.0, v30
	v_mfma_f32_32x32x2_f32 v[2:17], v192, v118, v[2:17]
	v_add_f32_e32 v36, 1.0, v36
	v_add_f32_e32 v42, 1.0, v42
	v_rcp_f32_e32 v24, v24
	v_rcp_f32_e32 v30, v30
	v_mfma_f32_32x32x2_f32 v[2:17], v193, v119, v[2:17]
	v_rcp_f32_e32 v36, v36
	v_rcp_f32_e32 v42, v42
	v_mul_f32_e32 v120, v64, v24
	v_mul_f32_e32 v121, v65, v30
	v_mul_f32_e32 v122, v66, v36
	v_mul_f32_e32 v123, v67, v42
	v_mul_f32_e32 v24, 0xbfb8aa3b, v68
	v_mul_f32_e32 v30, 0xbfb8aa3b, v69
	v_mfma_f32_32x32x2_f32 v[2:17], v194, v120, v[2:17]
	v_mul_f32_e32 v36, 0xbfb8aa3b, v70
	v_mul_f32_e32 v42, 0xbfb8aa3b, v71
	v_exp_f32_e32 v24, v24
	v_exp_f32_e32 v30, v30
	v_mfma_f32_32x32x2_f32 v[2:17], v195, v121, v[2:17]
	v_exp_f32_e32 v36, v36
	v_exp_f32_e32 v42, v42
	v_add_f32_e32 v24, 1.0, v24
	v_add_f32_e32 v30, 1.0, v30
	v_mfma_f32_32x32x2_f32 v[2:17], v196, v122, v[2:17]
	v_add_f32_e32 v36, 1.0, v36
	v_add_f32_e32 v42, 1.0, v42
	v_rcp_f32_e32 v24, v24
	v_rcp_f32_e32 v30, v30
	v_mfma_f32_32x32x2_f32 v[2:17], v197, v123, v[2:17]
	v_rcp_f32_e32 v36, v36
	v_rcp_f32_e32 v42, v42
	v_mul_f32_e32 v116, v68, v24
	v_mul_f32_e32 v117, v69, v30
	v_mul_f32_e32 v118, v70, v36
	v_mul_f32_e32 v119, v71, v42
	v_mul_f32_e32 v24, 0xbfb8aa3b, v72
	v_mul_f32_e32 v30, 0xbfb8aa3b, v73
	v_mfma_f32_32x32x2_f32 v[2:17], v198, v116, v[2:17]
	v_mul_f32_e32 v36, 0xbfb8aa3b, v74
	v_mul_f32_e32 v42, 0xbfb8aa3b, v75
	v_exp_f32_e32 v24, v24
	v_exp_f32_e32 v30, v30
	v_mfma_f32_32x32x2_f32 v[2:17], v199, v117, v[2:17]
	v_exp_f32_e32 v36, v36
	v_exp_f32_e32 v42, v42
	v_add_f32_e32 v24, 1.0, v24
	v_add_f32_e32 v30, 1.0, v30
	v_mfma_f32_32x32x2_f32 v[2:17], v200, v118, v[2:17]
	v_add_f32_e32 v36, 1.0, v36
	v_add_f32_e32 v42, 1.0, v42
	v_rcp_f32_e32 v24, v24
	v_rcp_f32_e32 v30, v30
	v_mfma_f32_32x32x2_f32 v[2:17], v201, v119, v[2:17]
	v_rcp_f32_e32 v36, v36
	v_rcp_f32_e32 v42, v42
	v_mul_f32_e32 v120, v72, v24
	v_mul_f32_e32 v121, v73, v30
	v_mul_f32_e32 v122, v74, v36
	v_mul_f32_e32 v123, v75, v42
	v_mul_f32_e32 v24, 0xbfb8aa3b, v76
	v_mul_f32_e32 v30, 0xbfb8aa3b, v77
	v_mfma_f32_32x32x2_f32 v[2:17], v202, v120, v[2:17]
	v_mul_f32_e32 v36, 0xbfb8aa3b, v78
	v_mul_f32_e32 v42, 0xbfb8aa3b, v79
	v_exp_f32_e32 v24, v24
	v_exp_f32_e32 v30, v30
	v_mfma_f32_32x32x2_f32 v[2:17], v203, v121, v[2:17]
	v_exp_f32_e32 v36, v36
	v_exp_f32_e32 v42, v42
	v_add_f32_e32 v24, 1.0, v24
	v_add_f32_e32 v30, 1.0, v30
	v_mfma_f32_32x32x2_f32 v[2:17], v204, v122, v[2:17]
	v_add_f32_e32 v36, 1.0, v36
	v_add_f32_e32 v42, 1.0, v42
	v_rcp_f32_e32 v24, v24
	v_rcp_f32_e32 v30, v30
	v_mfma_f32_32x32x2_f32 v[2:17], v205, v123, v[2:17]
	v_rcp_f32_e32 v36, v36
	v_rcp_f32_e32 v42, v42
	v_mul_f32_e32 v116, v76, v24
	v_mul_f32_e32 v117, v77, v30
	v_mul_f32_e32 v118, v78, v36
	v_mul_f32_e32 v119, v79, v42
	v_mul_f32_e32 v24, 0xbfb8aa3b, v80
	v_mul_f32_e32 v30, 0xbfb8aa3b, v81
	v_mfma_f32_32x32x2_f32 v[2:17], v206, v116, v[2:17]
	v_mul_f32_e32 v36, 0xbfb8aa3b, v82
	v_mul_f32_e32 v42, 0xbfb8aa3b, v83
	v_exp_f32_e32 v24, v24
	v_exp_f32_e32 v30, v30
	v_mfma_f32_32x32x2_f32 v[2:17], v207, v117, v[2:17]
	v_exp_f32_e32 v36, v36
	v_exp_f32_e32 v42, v42
	v_add_f32_e32 v24, 1.0, v24
	v_add_f32_e32 v30, 1.0, v30
	v_mfma_f32_32x32x2_f32 v[2:17], v208, v118, v[2:17]
	v_add_f32_e32 v36, 1.0, v36
	v_add_f32_e32 v42, 1.0, v42
	v_rcp_f32_e32 v24, v24
	v_rcp_f32_e32 v30, v30
	v_mfma_f32_32x32x2_f32 v[2:17], v209, v119, v[2:17]
	v_rcp_f32_e32 v36, v36
	v_rcp_f32_e32 v42, v42
	v_mul_f32_e32 v120, v80, v24
	v_mul_f32_e32 v121, v81, v30
	v_mul_f32_e32 v122, v82, v36
	v_mul_f32_e32 v123, v83, v42
	s_nop 1
	v_mfma_f32_32x32x2_f32 v[2:17], v210, v120, v[2:17]
	v_mfma_f32_32x32x2_f32 v[2:17], v211, v121, v[2:17]
	v_mfma_f32_32x32x2_f32 v[2:17], v212, v122, v[2:17]
	v_mfma_f32_32x32x2_f32 v[2:17], v213, v123, v[2:17]
	s_waitcnt vmcnt(0)
	s_cmp_eq_u32 s100, 1
	s_cbranch_scc1 .Lmod_skip
	global_load_dwordx4 v[52:55], v[22:23], off offset:456
	global_load_dword v182, v20, s[98:99]
	s_add_u32 s98, s98, 0x6000
	s_addc_u32 s99, s99, 0
	global_load_dword v183, v20, s[98:99]
	s_add_u32 s98, s98, 0x6000
	s_addc_u32 s99, s99, 0
	global_load_dword v184, v20, s[98:99]
	s_add_u32 s98, s98, 0x6000
	s_addc_u32 s99, s99, 0
	global_load_dword v185, v20, s[98:99]
	s_add_u32 s98, s98, 0x1e000
	s_addc_u32 s99, s99, 0
	global_load_dwordx4 v[56:59], v[22:23], off offset:488
	global_load_dword v186, v20, s[98:99]
	s_add_u32 s98, s98, 0x6000
	s_addc_u32 s99, s99, 0
	global_load_dword v187, v20, s[98:99]
	s_add_u32 s98, s98, 0x6000
	s_addc_u32 s99, s99, 0
	global_load_dword v188, v20, s[98:99]
	s_add_u32 s98, s98, 0x6000
	s_addc_u32 s99, s99, 0
	global_load_dword v189, v20, s[98:99]
	s_add_u32 s98, s98, 0x1e000
	s_addc_u32 s99, s99, 0
	global_load_dwordx4 v[60:63], v[22:23], off offset:520
	global_load_dword v190, v20, s[98:99]
	s_add_u32 s98, s98, 0x6000
	s_addc_u32 s99, s99, 0
	global_load_dword v191, v20, s[98:99]
	s_add_u32 s98, s98, 0x6000
	s_addc_u32 s99, s99, 0
	global_load_dword v192, v20, s[98:99]
	s_add_u32 s98, s98, 0x6000
	s_addc_u32 s99, s99, 0
	global_load_dword v193, v20, s[98:99]
	s_add_u32 s98, s98, 0x1e000
	s_addc_u32 s99, s99, 0
	global_load_dwordx4 v[64:67], v[22:23], off offset:552
	global_load_dword v194, v20, s[98:99]
	s_add_u32 s98, s98, 0x6000
	s_addc_u32 s99, s99, 0
	global_load_dword v195, v20, s[98:99]
	s_add_u32 s98, s98, 0x6000
	s_addc_u32 s99, s99, 0
	global_load_dword v196, v20, s[98:99]
	s_add_u32 s98, s98, 0x6000
	s_addc_u32 s99, s99, 0
	global_load_dword v197, v20, s[98:99]
	s_add_u32 s98, s98, 0x1e000
	s_addc_u32 s99, s99, 0
	global_load_dwordx4 v[68:71], v[22:23], off offset:584
	global_load_dword v198, v20, s[98:99]
	s_add_u32 s98, s98, 0x6000
	s_addc_u32 s99, s99, 0
	global_load_dword v199, v20, s[98:99]
	s_add_u32 s98, s98, 0x6000
	s_addc_u32 s99, s99, 0
	global_load_dword v200, v20, s[98:99]
	s_add_u32 s98, s98, 0x6000
	s_addc_u32 s99, s99, 0
	global_load_dword v201, v20, s[98:99]
	s_add_u32 s98, s98, 0x1e000
	s_addc_u32 s99, s99, 0
	global_load_dwordx4 v[72:75], v[22:23], off offset:616
	global_load_dword v202, v20, s[98:99]
	s_add_u32 s98, s98, 0x6000
	s_addc_u32 s99, s99, 0
	global_load_dword v203, v20, s[98:99]
	s_add_u32 s98, s98, 0x6000
	s_addc_u32 s99, s99, 0
	global_load_dword v204, v20, s[98:99]
	s_add_u32 s98, s98, 0x6000
	s_addc_u32 s99, s99, 0
	global_load_dword v205, v20, s[98:99]
	s_add_u32 s98, s98, 0x1e000
	s_addc_u32 s99, s99, 0
	global_load_dwordx4 v[76:79], v[22:23], off offset:648
	global_load_dword v206, v20, s[98:99]
	s_add_u32 s98, s98, 0x6000
	s_addc_u32 s99, s99, 0
	global_load_dword v207, v20, s[98:99]
	s_add_u32 s98, s98, 0x6000
	s_addc_u32 s99, s99, 0
	global_load_dword v208, v20, s[98:99]
	s_add_u32 s98, s98, 0x6000
	s_addc_u32 s99, s99, 0
	global_load_dword v209, v20, s[98:99]
	s_add_u32 s98, s98, 0x1e000
	s_addc_u32 s99, s99, 0
	global_load_dwordx4 v[80:83], v[22:23], off offset:680
	global_load_dword v210, v20, s[98:99]
	s_add_u32 s98, s98, 0x6000
	s_addc_u32 s99, s99, 0
	global_load_dword v211, v20, s[98:99]
	s_add_u32 s98, s98, 0x6000
	s_addc_u32 s99, s99, 0
	global_load_dword v212, v20, s[98:99]
	s_add_u32 s98, s98, 0x6000
	s_addc_u32 s99, s99, 0
	global_load_dword v213, v20, s[98:99]
	s_add_u32 s98, s98, 0x1e000
	s_addc_u32 s99, s99, 0
.Lmod_skip:
	v_mul_f32_e32 v24, 0xbfb8aa3b, v84
	v_mul_f32_e32 v30, 0xbfb8aa3b, v85
	v_mul_f32_e32 v36, 0xbfb8aa3b, v86
	v_mul_f32_e32 v42, 0xbfb8aa3b, v87
	v_exp_f32_e32 v24, v24
	v_exp_f32_e32 v30, v30
	v_exp_f32_e32 v36, v36
	v_exp_f32_e32 v42, v42
	v_add_f32_e32 v24, 1.0, v24
	v_add_f32_e32 v30, 1.0, v30
	v_add_f32_e32 v36, 1.0, v36
	v_add_f32_e32 v42, 1.0, v42
	v_rcp_f32_e32 v24, v24
	v_rcp_f32_e32 v30, v30
	v_rcp_f32_e32 v36, v36
	v_rcp_f32_e32 v42, v42
	v_mul_f32_e32 v116, v84, v24
	v_mul_f32_e32 v117, v85, v30
	v_mul_f32_e32 v118, v86, v36
	v_mul_f32_e32 v119, v87, v42
	v_mul_f32_e32 v24, 0xbfb8aa3b, v88
	v_mul_f32_e32 v30, 0xbfb8aa3b, v89
	v_mfma_f32_32x32x2_f32 v[2:17], v214, v116, v[2:17]
	v_mul_f32_e32 v36, 0xbfb8aa3b, v90
	v_mul_f32_e32 v42, 0xbfb8aa3b, v91
	v_exp_f32_e32 v24, v24
	v_exp_f32_e32 v30, v30
	v_mfma_f32_32x32x2_f32 v[2:17], v215, v117, v[2:17]
	v_exp_f32_e32 v36, v36
	v_exp_f32_e32 v42, v42
	v_add_f32_e32 v24, 1.0, v24
	v_add_f32_e32 v30, 1.0, v30
	v_mfma_f32_32x32x2_f32 v[2:17], v216, v118, v[2:17]
	v_add_f32_e32 v36, 1.0, v36
	v_add_f32_e32 v42, 1.0, v42
	v_rcp_f32_e32 v24, v24
	v_rcp_f32_e32 v30, v30
	v_mfma_f32_32x32x2_f32 v[2:17], v217, v119, v[2:17]
	v_rcp_f32_e32 v36, v36
	v_rcp_f32_e32 v42, v42
	v_mul_f32_e32 v120, v88, v24
	v_mul_f32_e32 v121, v89, v30
	v_mul_f32_e32 v122, v90, v36
	v_mul_f32_e32 v123, v91, v42
	v_mul_f32_e32 v24, 0xbfb8aa3b, v92
	v_mul_f32_e32 v30, 0xbfb8aa3b, v93
	v_mfma_f32_32x32x2_f32 v[2:17], v218, v120, v[2:17]
	v_mul_f32_e32 v36, 0xbfb8aa3b, v94
	v_mul_f32_e32 v42, 0xbfb8aa3b, v95
	v_exp_f32_e32 v24, v24
	v_exp_f32_e32 v30, v30
	v_mfma_f32_32x32x2_f32 v[2:17], v219, v121, v[2:17]
	v_exp_f32_e32 v36, v36
	v_exp_f32_e32 v42, v42
	v_add_f32_e32 v24, 1.0, v24
	v_add_f32_e32 v30, 1.0, v30
	v_mfma_f32_32x32x2_f32 v[2:17], v220, v122, v[2:17]
	v_add_f32_e32 v36, 1.0, v36
	v_add_f32_e32 v42, 1.0, v42
	v_rcp_f32_e32 v24, v24
	v_rcp_f32_e32 v30, v30
	v_mfma_f32_32x32x2_f32 v[2:17], v221, v123, v[2:17]
	v_rcp_f32_e32 v36, v36
	v_rcp_f32_e32 v42, v42
	v_mul_f32_e32 v116, v92, v24
	v_mul_f32_e32 v117, v93, v30
	v_mul_f32_e32 v118, v94, v36
	v_mul_f32_e32 v119, v95, v42
	v_mul_f32_e32 v24, 0xbfb8aa3b, v96
	v_mul_f32_e32 v30, 0xbfb8aa3b, v97
	v_mfma_f32_32x32x2_f32 v[2:17], v222, v116, v[2:17]
	v_mul_f32_e32 v36, 0xbfb8aa3b, v98
	v_mul_f32_e32 v42, 0xbfb8aa3b, v99
	v_exp_f32_e32 v24, v24
	v_exp_f32_e32 v30, v30
	v_mfma_f32_32x32x2_f32 v[2:17], v223, v117, v[2:17]
	v_exp_f32_e32 v36, v36
	v_exp_f32_e32 v42, v42
	v_add_f32_e32 v24, 1.0, v24
	v_add_f32_e32 v30, 1.0, v30
	v_mfma_f32_32x32x2_f32 v[2:17], v224, v118, v[2:17]
	v_add_f32_e32 v36, 1.0, v36
	v_add_f32_e32 v42, 1.0, v42
	v_rcp_f32_e32 v24, v24
	v_rcp_f32_e32 v30, v30
	v_mfma_f32_32x32x2_f32 v[2:17], v225, v119, v[2:17]
	v_rcp_f32_e32 v36, v36
	v_rcp_f32_e32 v42, v42
	v_mul_f32_e32 v120, v96, v24
	v_mul_f32_e32 v121, v97, v30
	v_mul_f32_e32 v122, v98, v36
	v_mul_f32_e32 v123, v99, v42
	v_mul_f32_e32 v24, 0xbfb8aa3b, v100
	v_mul_f32_e32 v30, 0xbfb8aa3b, v101
	v_mfma_f32_32x32x2_f32 v[2:17], v226, v120, v[2:17]
	v_mul_f32_e32 v36, 0xbfb8aa3b, v102
	v_mul_f32_e32 v42, 0xbfb8aa3b, v103
	v_exp_f32_e32 v24, v24
	v_exp_f32_e32 v30, v30
	v_mfma_f32_32x32x2_f32 v[2:17], v227, v121, v[2:17]
	v_exp_f32_e32 v36, v36
	v_exp_f32_e32 v42, v42
	v_add_f32_e32 v24, 1.0, v24
	v_add_f32_e32 v30, 1.0, v30
	v_mfma_f32_32x32x2_f32 v[2:17], v228, v122, v[2:17]
	v_add_f32_e32 v36, 1.0, v36
	v_add_f32_e32 v42, 1.0, v42
	v_rcp_f32_e32 v24, v24
	v_rcp_f32_e32 v30, v30
	v_mfma_f32_32x32x2_f32 v[2:17], v229, v123, v[2:17]
	v_rcp_f32_e32 v36, v36
	v_rcp_f32_e32 v42, v42
	v_mul_f32_e32 v116, v100, v24
	v_mul_f32_e32 v117, v101, v30
	v_mul_f32_e32 v118, v102, v36
	v_mul_f32_e32 v119, v103, v42
	v_mul_f32_e32 v24, 0xbfb8aa3b, v104
	v_mul_f32_e32 v30, 0xbfb8aa3b, v105
	v_mfma_f32_32x32x2_f32 v[2:17], v230, v116, v[2:17]
	v_mul_f32_e32 v36, 0xbfb8aa3b, v106
	v_mul_f32_e32 v42, 0xbfb8aa3b, v107
	v_exp_f32_e32 v24, v24
	v_exp_f32_e32 v30, v30
	v_mfma_f32_32x32x2_f32 v[2:17], v231, v117, v[2:17]
	v_exp_f32_e32 v36, v36
	v_exp_f32_e32 v42, v42
	v_add_f32_e32 v24, 1.0, v24
	v_add_f32_e32 v30, 1.0, v30
	v_mfma_f32_32x32x2_f32 v[2:17], v232, v118, v[2:17]
	v_add_f32_e32 v36, 1.0, v36
	v_add_f32_e32 v42, 1.0, v42
	v_rcp_f32_e32 v24, v24
	v_rcp_f32_e32 v30, v30
	v_mfma_f32_32x32x2_f32 v[2:17], v233, v119, v[2:17]
	v_rcp_f32_e32 v36, v36
	v_rcp_f32_e32 v42, v42
	v_mul_f32_e32 v120, v104, v24
	v_mul_f32_e32 v121, v105, v30
	v_mul_f32_e32 v122, v106, v36
	v_mul_f32_e32 v123, v107, v42
	v_mul_f32_e32 v24, 0xbfb8aa3b, v108
	v_mul_f32_e32 v30, 0xbfb8aa3b, v109
	v_mfma_f32_32x32x2_f32 v[2:17], v234, v120, v[2:17]
	v_mul_f32_e32 v36, 0xbfb8aa3b, v110
	v_mul_f32_e32 v42, 0xbfb8aa3b, v111
	v_exp_f32_e32 v24, v24
	v_exp_f32_e32 v30, v30
	v_mfma_f32_32x32x2_f32 v[2:17], v235, v121, v[2:17]
	v_exp_f32_e32 v36, v36
	v_exp_f32_e32 v42, v42
	v_add_f32_e32 v24, 1.0, v24
	v_add_f32_e32 v30, 1.0, v30
	v_mfma_f32_32x32x2_f32 v[2:17], v236, v122, v[2:17]
	v_add_f32_e32 v36, 1.0, v36
	v_add_f32_e32 v42, 1.0, v42
	v_rcp_f32_e32 v24, v24
	v_rcp_f32_e32 v30, v30
	v_mfma_f32_32x32x2_f32 v[2:17], v237, v123, v[2:17]
	v_rcp_f32_e32 v36, v36
	v_rcp_f32_e32 v42, v42
	v_mul_f32_e32 v116, v108, v24
	v_mul_f32_e32 v117, v109, v30
	v_mul_f32_e32 v118, v110, v36
	v_mul_f32_e32 v119, v111, v42
	v_mul_f32_e32 v24, 0xbfb8aa3b, v112
	v_mul_f32_e32 v30, 0xbfb8aa3b, v113
	v_mfma_f32_32x32x2_f32 v[2:17], v238, v116, v[2:17]
	v_mul_f32_e32 v36, 0xbfb8aa3b, v114
	v_mul_f32_e32 v42, 0xbfb8aa3b, v115
	v_exp_f32_e32 v24, v24
	v_exp_f32_e32 v30, v30
	v_mfma_f32_32x32x2_f32 v[2:17], v239, v117, v[2:17]
	v_exp_f32_e32 v36, v36
	v_exp_f32_e32 v42, v42
	v_add_f32_e32 v24, 1.0, v24
	v_add_f32_e32 v30, 1.0, v30
	v_mfma_f32_32x32x2_f32 v[2:17], v240, v118, v[2:17]
	v_add_f32_e32 v36, 1.0, v36
	v_add_f32_e32 v42, 1.0, v42
	v_rcp_f32_e32 v24, v24
	v_rcp_f32_e32 v30, v30
	v_mfma_f32_32x32x2_f32 v[2:17], v241, v119, v[2:17]
	v_rcp_f32_e32 v36, v36
	v_rcp_f32_e32 v42, v42
	v_mul_f32_e32 v120, v112, v24
	v_mul_f32_e32 v121, v113, v30
	v_mul_f32_e32 v122, v114, v36
	v_mul_f32_e32 v123, v115, v42
	s_nop 1
	v_mfma_f32_32x32x2_f32 v[2:17], v242, v120, v[2:17]
	v_mfma_f32_32x32x2_f32 v[2:17], v243, v121, v[2:17]
	v_mfma_f32_32x32x2_f32 v[2:17], v244, v122, v[2:17]
	v_mfma_f32_32x32x2_f32 v[2:17], v245, v123, v[2:17]
	v_lshl_add_u64 v[22:23], v[22:23], 0, v[48:49]
	s_add_i32 s100, s100, 1
	s_cmp_lt_u32 s100, 2
	s_cbranch_scc1 .Lmod_loop
	s_lshl_b32 s4, s80, 3
	s_andn2_b32 s4, s4, 31
	s_ashr_i32 s5, s4, 31
	v_lshl_add_u64 v[18:19], s[4:5], 2, v[146:147]
	s_nop 15
	s_nop 3
	global_store_dwordx4 v[18:19], v[2:5], off
	global_store_dwordx4 v[18:19], v[6:9], off offset:32
	global_store_dwordx4 v[18:19], v[10:13], off offset:64
	global_store_dwordx4 v[18:19], v[14:17], off offset:96
	s_branch .LBB0_11

.LBB0_294:
	s_cmp_lt_i32 s46, 4
	s_cselect_b64 s[0:1], -1, 0
	s_and_b64 s[38:39], s[0:1], s[4:5]
	s_andn2_b64 vcc, exec, s[38:39]
	s_cbranch_vccnz .LBB0_463
	s_mov_b64 s[34:35], s[52:53]
	s_load_dwordx4 s[28:31], s[34:35], 0xd0
	v_mov_b32_e32 v219, v0
	s_waitcnt lgkmcnt(0)
	s_add_u32 s40, s30, 0x21e00000
	s_addc_u32 s41, s31, 0
	s_cmpk_gt_i32 s78, 0x7ff
	v_and_b32_e32 v254, 63, v219
	s_cbranch_scc1 .LBB0_317
	s_waitcnt vmcnt(0)
	s_load_dwordx2 s[12:13], s[34:35], 0x30
	v_and_b32_e32 v34, 15, v219
	v_lshrrev_b32_e32 v35, 4, v219
	v_lshlrev_b32_e32 v36, 12, v35
	v_lshl_add_u32 v36, v34, 4, v36
	v_add_u32_e32 v37, 0x20000, v36
	v_add_u32_e32 v38, 0x40000, v36
	v_add_u32_e32 v39, 0x60000, v36
	v_add_u32_e32 v40, 0x80, v35
	v_min_u32_e32 v40, 0x8e, v40
	v_lshlrev_b32_e32 v40, 12, v40
	v_lshl_add_u32 v40, v34, 4, v40
	v_max_u32_e32 v41, 15, v35
	v_lshlrev_b32_e32 v41, 12, v41
	v_lshl_add_u32 v41, v34, 4, v41
	v_cmp_gt_u32_e64 s[4:5], 15, v35
	v_cmp_gt_u32_e32 vcc, 0xf0, v219
	s_mov_b64 s[6:7], vcc
	v_lshlrev_b32_e32 v42, 4, v219
	v_and_b32_e32 v43, 0x7f, v219
	v_lshlrev_b32_e32 v43, 1, v43
	s_lshr_b32 s8, s97, 1
	s_lshl_b32 s9, s8, 13
	v_add_u32_e32 v44, s9, v43
	v_add_u32_e32 v45, 0xf00, v44
	s_mul_i32 s9, s8, 0x2200
	v_add_u32_e32 v47, s9, v43
	v_add_u32_e32 v47, 0x9000, v47
	v_and_b32_e32 v48, 31, v254
	v_lshrrev_b32_e32 v49, 5, v254
	s_and_b32 s9, s97, 3
	s_lshr_b32 s10, s97, 2
	s_lshl_b32 s11, s9, 5
	v_add_u32_e32 v50, s11, v48
	v_mul_u32_u24_e32 v51, 0x110, v50
	v_lshl_add_u32 v51, v49, 4, v51
	v_add_u32_e32 v51, 0x9000, v51
	s_lshl_b32 s11, s10, 6
	v_add_u32_e32 v52, s11, v48
	v_mul_u32_u24_e32 v52, 0x110, v52
	v_lshl_add_u32 v52, v49, 4, v52
	v_add_u32_e32 v52, 0x11800, v52
	v_mul_u32_u24_e32 v53, 0x110, v35
	v_lshl_add_u32 v53, v34, 4, v53
	v_add_u32_e32 v53, 0x11800, v53
	v_lshlrev_b32_e32 v54, 10, v50
	v_add_u32_e32 v54, s11, v54
	v_lshl_add_u32 v54, v49, 3, v54
	v_mov_b32_e32 v55, 0x43e00000
	v_mov_b32_e32 v195, 0
	v_lshlrev_b32_e32 v196, 4, v49
	s_mov_b32 s100, 0xc3e00000
	s_mov_b32 s14, s78
	s_mov_b32 s15, -1
	s_mov_b32 s21, 0
	s_and_b32 s23, s14, 3
	s_lshr_b32 s24, s14, 2
	s_lshl_b32 s24, s24, 7
	s_and_b32 s25, s24, 0x7ff
	s_sub_i32 s24, s24, 15
	s_ashr_i32 s27, s24, 31
	s_mov_b32 s26, s24
	s_lshl_b64 s[26:27], s[26:27], 12
	s_add_u32 s26, s26, s28
	s_addc_u32 s27, s27, s29
	s_lshl_b32 s23, s23, 8
	s_add_u32 s26, s26, s23
	s_addc_u32 s27, s27, 0
	v_mov_b32_e32 v1, v36
	s_cmp_lg_u32 s25, 0
	s_cbranch_scc1 .Lpool_nz_56_s14
	v_mov_b32_e32 v1, v41
.Lpool_nz_56_s14:
	s_nop 0
	global_load_dwordx4 v[56:59], v1, s[26:27]
	global_load_dwordx4 v[60:63], v37, s[26:27]
	global_load_dwordx4 v[64:67], v38, s[26:27]
	global_load_dwordx4 v[68:71], v39, s[26:27]
	global_load_dwordx4 v[72:75], v40, s[26:27]
	s_add_i32 s22, s14, s72
	s_cmpk_lt_u32 s22, 0x800
	s_cselect_b32 s22, s22, s14
	s_and_b32 s23, s22, 3
	s_lshr_b32 s24, s22, 2
	s_lshl_b32 s24, s24, 7
	s_and_b32 s25, s24, 0x7ff
	s_sub_i32 s24, s24, 15
	s_ashr_i32 s27, s24, 31
	s_mov_b32 s26, s24
	s_lshl_b64 s[26:27], s[26:27], 12
	s_add_u32 s26, s26, s28
	s_addc_u32 s27, s27, s29
	s_lshl_b32 s23, s23, 8
	s_add_u32 s26, s26, s23
	s_addc_u32 s27, s27, 0
	v_mov_b32_e32 v1, v36
	s_cmp_lg_u32 s25, 0
	s_cbranch_scc1 .Lpool_nz_76_s22
	v_mov_b32_e32 v1, v41
.Lpool_nz_76_s22:
	s_nop 0
	global_load_dwordx4 v[76:79], v1, s[26:27]
	global_load_dwordx4 v[80:83], v37, s[26:27]
	global_load_dwordx4 v[84:87], v38, s[26:27]
	global_load_dwordx4 v[88:91], v39, s[26:27]
	global_load_dwordx4 v[92:95], v40, s[26:27]
.Lpool_unit:
	s_and_b32 s16, s14, 3
	s_cmp_eq_u32 s16, s15
	s_cbranch_scc1 .Lpool_same_g
	s_barrier
	s_mov_b32 s15, s16
	s_lshl_b32 s22, s16, 15
	s_add_u32 s18, s30, 0xd00000
	s_addc_u32 s19, s31, 0
	s_add_u32 s18, s18, s22
	s_addc_u32 s19, s19, 0
	global_load_dwordx4 v[2:5], v42, s[18:19]
	s_add_u32 s18, s18, 0x2000
	s_addc_u32 s19, s19, 0
	global_load_dwordx4 v[6:9], v42, s[18:19]
	s_add_u32 s18, s18, 0x2000
	s_addc_u32 s19, s19, 0
	global_load_dwordx4 v[10:13], v42, s[18:19]
	s_add_u32 s18, s18, 0x2000
	s_addc_u32 s19, s19, 0
	global_load_dwordx4 v[14:17], v42, s[18:19]
	s_waitcnt lgkmcnt(0)
	s_lshl_b32 s22, s16, 9
	s_lshl_b32 s23, s10, 8
	s_add_i32 s22, s22, s23
	s_add_u32 s18, s12, s22
	s_addc_u32 s19, s13, 0
	global_load_dwordx4 v[96:99], v196, s[18:19] offset:0
	global_load_dwordx4 v[100:103], v196, s[18:19] offset:32
	global_load_dwordx4 v[104:107], v196, s[18:19] offset:64
	global_load_dwordx4 v[108:111], v196, s[18:19] offset:96
	global_load_dwordx4 v[112:115], v196, s[18:19] offset:128
	global_load_dwordx4 v[116:119], v196, s[18:19] offset:160
	global_load_dwordx4 v[120:123], v196, s[18:19] offset:192
	global_load_dwordx4 v[124:127], v196, s[18:19] offset:224
	s_waitcnt vmcnt(8)
	ds_write_b128 v53, v[2:5]
	ds_write_b128 v53, v[6:9] offset:8704
	ds_write_b128 v53, v[10:13] offset:17408
	ds_write_b128 v53, v[14:17] offset:26112
	s_waitcnt vmcnt(0) lgkmcnt(0)
	s_barrier
	ds_read_b128 v[128:131], v52
	ds_read_b128 v[132:135], v52 offset:32
	ds_read_b128 v[136:139], v52 offset:64
	ds_read_b128 v[140:143], v52 offset:96
	ds_read_b128 v[144:147], v52 offset:128
	ds_read_b128 v[148:151], v52 offset:160
	ds_read_b128 v[152:155], v52 offset:192
	ds_read_b128 v[156:159], v52 offset:224
	ds_read_b128 v[160:163], v52 offset:8704
	ds_read_b128 v[164:167], v52 offset:8736
	ds_read_b128 v[168:171], v52 offset:8768
	ds_read_b128 v[172:175], v52 offset:8800
	ds_read_b128 v[176:179], v52 offset:8832
	ds_read_b128 v[180:183], v52 offset:8864
	ds_read_b128 v[184:187], v52 offset:8896
	ds_read_b128 v[188:191], v52 offset:8928
.Lpool_same_g:
	s_lshl_b32 s99, 2, s16
	s_sub_i32 s98, 0x7e, s16
	s_lshl_b32 s98, s98, 23
	s_lshr_b32 s17, s14, 2
	s_lshl_b32 s17, s17, 7
	s_and_b32 s20, s17, 0x7ff
	s_lshl_b32 s22, s72, 1
	s_add_i32 s22, s22, s14
	s_cmpk_lt_u32 s22, 0x800
	s_cselect_b32 s22, s22, s14
	s_mov_b32 s101, s22
	s_waitcnt vmcnt(13)
	s_bitcmp1_b32 s21, 0
	s_cbranch_scc1 .Lpool_odd
	s_cmp_lg_u32 s20, 0
	s_cbranch_scc1 .Lpool_nozero_0
	v_cndmask_b32_e64 v56, v56, 0, s[4:5]
	v_cndmask_b32_e64 v57, v57, 0, s[4:5]
	v_cndmask_b32_e64 v58, v58, 0, s[4:5]
	v_cndmask_b32_e64 v59, v59, 0, s[4:5]
.Lpool_nozero_0:
	ds_write_b128 v42, v[56:59]
	ds_write_b128 v42, v[60:63] offset:8192
	ds_write_b128 v42, v[64:67] offset:16384
	ds_write_b128 v42, v[68:71] offset:24576
	s_mov_b64 s[0:1], exec
	s_and_b64 exec, exec, s[6:7]
	ds_write_b128 v42, v[72:75] offset:32768
	s_mov_b64 exec, s[0:1]
	s_and_b32 s23, s101, 3
	s_lshr_b32 s24, s101, 2
	s_lshl_b32 s24, s24, 7
	s_and_b32 s25, s24, 0x7ff
	s_sub_i32 s24, s24, 15
	s_ashr_i32 s27, s24, 31
	s_mov_b32 s26, s24
	s_lshl_b64 s[26:27], s[26:27], 12
	s_add_u32 s26, s26, s28
	s_addc_u32 s27, s27, s29
	s_lshl_b32 s23, s23, 8
	s_add_u32 s26, s26, s23
	s_addc_u32 s27, s27, 0
	v_mov_b32_e32 v1, v36
	s_cmp_lg_u32 s25, 0
	s_cbranch_scc1 .Lpool_nz_56_s101
	v_mov_b32_e32 v1, v41
.Lpool_nz_56_s101:
	s_nop 0
	global_load_dwordx4 v[56:59], v1, s[26:27]
	global_load_dwordx4 v[60:63], v37, s[26:27]
	global_load_dwordx4 v[64:67], v38, s[26:27]
	global_load_dwordx4 v[68:71], v39, s[26:27]
	global_load_dwordx4 v[72:75], v40, s[26:27]
	s_branch .Lpool_join
.Lpool_odd:
	s_cmp_lg_u32 s20, 0
	s_cbranch_scc1 .Lpool_nozero_1
	v_cndmask_b32_e64 v76, v76, 0, s[4:5]
	v_cndmask_b32_e64 v77, v77, 0, s[4:5]
	v_cndmask_b32_e64 v78, v78, 0, s[4:5]
	v_cndmask_b32_e64 v79, v79, 0, s[4:5]
.Lpool_nozero_1:
	ds_write_b128 v42, v[76:79]
	ds_write_b128 v42, v[80:83] offset:8192
	ds_write_b128 v42, v[84:87] offset:16384
	ds_write_b128 v42, v[88:91] offset:24576
	s_mov_b64 s[0:1], exec
	s_and_b64 exec, exec, s[6:7]
	ds_write_b128 v42, v[92:95] offset:32768
	s_mov_b64 exec, s[0:1]
	s_and_b32 s23, s101, 3
	s_lshr_b32 s24, s101, 2
	s_lshl_b32 s24, s24, 7
	s_and_b32 s25, s24, 0x7ff
	s_sub_i32 s24, s24, 15
	s_ashr_i32 s27, s24, 31
	s_mov_b32 s26, s24
	s_lshl_b64 s[26:27], s[26:27], 12
	s_add_u32 s26, s26, s28
	s_addc_u32 s27, s27, s29
	s_lshl_b32 s23, s23, 8
	s_add_u32 s26, s26, s23
	s_addc_u32 s27, s27, 0
	v_mov_b32_e32 v1, v36
	s_cmp_lg_u32 s25, 0
	s_cbranch_scc1 .Lpool_nz_76_s101
	v_mov_b32_e32 v1, v41

.Lpool_join:
	s_waitcnt lgkmcnt(0)
	s_barrier
	s_sub_i32 s0, 16, s99
	s_lshl_b32 s0, s0, 8
	v_add_u32_e32 v46, s0, v44
	ds_read_u16 v197, v44 offset:3584
	ds_read_u16 v198, v44 offset:3328
	ds_read_u16 v199, v44 offset:3072
	ds_read_u16 v200, v44 offset:2816
	ds_read_u16 v201, v44 offset:2560
	ds_read_u16 v202, v44 offset:2304
	ds_read_u16 v203, v44 offset:2048
	ds_read_u16 v204, v44 offset:1792
	ds_read_u16 v205, v44 offset:1536
	ds_read_u16 v206, v44 offset:1280
	ds_read_u16 v207, v44 offset:1024
	ds_read_u16 v208, v44 offset:768
	ds_read_u16 v209, v44 offset:512
	ds_read_u16 v210, v44 offset:256
	ds_read_u16 v211, v44 offset:0
	ds_read_u16 v2, v45
	ds_read_u16 v220, v46
	ds_read_u16 v3, v45 offset:256
	ds_read_u16 v221, v46 offset:256
	ds_read_u16 v4, v45 offset:512
	ds_read_u16 v222, v46 offset:512
	ds_read_u16 v5, v45 offset:768
	ds_read_u16 v223, v46 offset:768
	ds_read_u16 v6, v45 offset:1024
	ds_read_u16 v224, v46 offset:1024
	ds_read_u16 v7, v45 offset:1280
	ds_read_u16 v225, v46 offset:1280
	ds_read_u16 v8, v45 offset:1536
	ds_read_u16 v226, v46 offset:1536
	ds_read_u16 v9, v45 offset:1792
	ds_read_u16 v227, v46 offset:1792
	ds_read_u16 v10, v45 offset:2048
	ds_read_u16 v228, v46 offset:2048
	ds_read_u16 v11, v45 offset:2304
	ds_read_u16 v229, v46 offset:2304
	ds_read_u16 v12, v45 offset:2560
	ds_read_u16 v230, v46 offset:2560
	ds_read_u16 v13, v45 offset:2816
	ds_read_u16 v231, v46 offset:2816
	ds_read_u16 v14, v45 offset:3072
	ds_read_u16 v232, v46 offset:3072
	ds_read_u16 v15, v45 offset:3328
	ds_read_u16 v233, v46 offset:3328
	ds_read_u16 v16, v45 offset:3584
	ds_read_u16 v234, v46 offset:3584
	ds_read_u16 v17, v45 offset:3840
	ds_read_u16 v235, v46 offset:3840
	ds_read_u16 v18, v45 offset:4096
	ds_read_u16 v236, v46 offset:4096
	ds_read_u16 v19, v45 offset:4352
	ds_read_u16 v237, v46 offset:4352
	ds_read_u16 v20, v45 offset:4608
	ds_read_u16 v238, v46 offset:4608
	ds_read_u16 v21, v45 offset:4864
	ds_read_u16 v239, v46 offset:4864
	ds_read_u16 v22, v45 offset:5120
	ds_read_u16 v240, v46 offset:5120
	ds_read_u16 v23, v45 offset:5376
	ds_read_u16 v241, v46 offset:5376
	ds_read_u16 v24, v45 offset:5632
	ds_read_u16 v242, v46 offset:5632
	ds_read_u16 v25, v45 offset:5888
	ds_read_u16 v243, v46 offset:5888
	ds_read_u16 v26, v45 offset:6144
	ds_read_u16 v244, v46 offset:6144
	ds_read_u16 v27, v45 offset:6400
	ds_read_u16 v245, v46 offset:6400
	ds_read_u16 v28, v45 offset:6656
	ds_read_u16 v246, v46 offset:6656
	ds_read_u16 v29, v45 offset:6912
	ds_read_u16 v247, v46 offset:6912
	ds_read_u16 v30, v45 offset:7168
	ds_read_u16 v248, v46 offset:7168
	ds_read_u16 v31, v45 offset:7424
	ds_read_u16 v249, v46 offset:7424
	ds_read_u16 v32, v45 offset:7680
	ds_read_u16 v250, v46 offset:7680
	ds_read_u16 v33, v45 offset:7936
	ds_read_u16 v251, v46 offset:7936
	s_lshl_b32 s0, s8, 5
	s_add_i32 s0, s0, s20
	s_cmp_eq_u32 s0, 0
	s_cselect_b32 s1, 1, 0
	v_mov_b32_e32 v192, 0
	s_waitcnt lgkmcnt(15)
	v_lshlrev_b32_e32 v197, 16, v197
	v_add_f32_e32 v192, v192, v197
	s_cmp_eq_u32 s99, 2
	s_cbranch_scc1 .Lpool_presum_done
	v_lshlrev_b32_e32 v198, 16, v198
	v_add_f32_e32 v192, v192, v198
	v_lshlrev_b32_e32 v199, 16, v199
	v_add_f32_e32 v192, v192, v199
	s_cmp_eq_u32 s99, 4
	s_cbranch_scc1 .Lpool_presum_done
	v_lshlrev_b32_e32 v200, 16, v200
	v_add_f32_e32 v192, v192, v200
	v_lshlrev_b32_e32 v201, 16, v201
	v_add_f32_e32 v192, v192, v201
	v_lshlrev_b32_e32 v202, 16, v202
	v_add_f32_e32 v192, v192, v202
	v_lshlrev_b32_e32 v203, 16, v203
	v_add_f32_e32 v192, v192, v203
	s_cmp_eq_u32 s99, 8
	s_cbranch_scc1 .Lpool_presum_done
	v_lshlrev_b32_e32 v204, 16, v204
	v_add_f32_e32 v192, v192, v204
	v_lshlrev_b32_e32 v205, 16, v205
	v_add_f32_e32 v192, v192, v205
	v_lshlrev_b32_e32 v206, 16, v206
	v_add_f32_e32 v192, v192, v206
	v_lshlrev_b32_e32 v207, 16, v207
	v_add_f32_e32 v192, v192, v207
	v_lshlrev_b32_e32 v208, 16, v208
	v_add_f32_e32 v192, v192, v208
	v_lshlrev_b32_e32 v209, 16, v209
	v_add_f32_e32 v192, v192, v209
	v_lshlrev_b32_e32 v210, 16, v210
	v_add_f32_e32 v192, v192, v210
	v_lshlrev_b32_e32 v211, 16, v211
	v_add_f32_e32 v192, v192, v211
.Lpool_presum_done:
	s_cmp_lg_u32 s1, 0
	s_cbranch_scc1 .Lpool_rows_special
	v_lshlrev_b32_e32 v2, 16, v2
	v_add_f32_e32 v192, v192, v2
	v_lshlrev_b32_e32 v220, 16, v220
	v_mul_f32_e32 v193, s98, v192
	v_sub_f32_e32 v193, v193, v2
	v_sub_f32_e32 v192, v192, v220
	v_cvt_pk_bf16_f32 v193, v193, v195
	ds_write_b16 v47, v193
	v_lshlrev_b32_e32 v3, 16, v3
	v_add_f32_e32 v192, v192, v3
	v_lshlrev_b32_e32 v221, 16, v221
	v_mul_f32_e32 v193, s98, v192
	v_sub_f32_e32 v193, v193, v3
	v_sub_f32_e32 v192, v192, v221
	v_cvt_pk_bf16_f32 v193, v193, v195
	ds_write_b16 v47, v193 offset:272
	v_lshlrev_b32_e32 v4, 16, v4
	v_add_f32_e32 v192, v192, v4
	v_lshlrev_b32_e32 v222, 16, v222
	v_mul_f32_e32 v193, s98, v192
	v_sub_f32_e32 v193, v193, v4
	v_sub_f32_e32 v192, v192, v222
	v_cvt_pk_bf16_f32 v193, v193, v195
	ds_write_b16 v47, v193 offset:544
	v_lshlrev_b32_e32 v5, 16, v5
	v_add_f32_e32 v192, v192, v5
	v_lshlrev_b32_e32 v223, 16, v223
	v_mul_f32_e32 v193, s98, v192
	v_sub_f32_e32 v193, v193, v5
	v_sub_f32_e32 v192, v192, v223
	v_cvt_pk_bf16_f32 v193, v193, v195
	ds_write_b16 v47, v193 offset:816
	v_lshlrev_b32_e32 v6, 16, v6
	v_add_f32_e32 v192, v192, v6
	v_lshlrev_b32_e32 v224, 16, v224
	v_mul_f32_e32 v193, s98, v192
	v_sub_f32_e32 v193, v193, v6
	v_sub_f32_e32 v192, v192, v224
	v_cvt_pk_bf16_f32 v193, v193, v195
	ds_write_b16 v47, v193 offset:1088
	v_lshlrev_b32_e32 v7, 16, v7
	v_add_f32_e32 v192, v192, v7
	v_lshlrev_b32_e32 v225, 16, v225
	v_mul_f32_e32 v193, s98, v192
	v_sub_f32_e32 v193, v193, v7
	v_sub_f32_e32 v192, v192, v225
	v_cvt_pk_bf16_f32 v193, v193, v195
	ds_write_b16 v47, v193 offset:1360
	v_lshlrev_b32_e32 v8, 16, v8
	v_add_f32_e32 v192, v192, v8
	v_lshlrev_b32_e32 v226, 16, v226
	v_mul_f32_e32 v193, s98, v192
	v_sub_f32_e32 v193, v193, v8
	v_sub_f32_e32 v192, v192, v226
	v_cvt_pk_bf16_f32 v193, v193, v195
	ds_write_b16 v47, v193 offset:1632
	v_lshlrev_b32_e32 v9, 16, v9
	v_add_f32_e32 v192, v192, v9
	v_lshlrev_b32_e32 v227, 16, v227
	v_mul_f32_e32 v193, s98, v192
	v_sub_f32_e32 v193, v193, v9
	v_sub_f32_e32 v192, v192, v227
	v_cvt_pk_bf16_f32 v193, v193, v195
	ds_write_b16 v47, v193 offset:1904
	v_lshlrev_b32_e32 v10, 16, v10
	v_add_f32_e32 v192, v192, v10
	v_lshlrev_b32_e32 v228, 16, v228
	v_mul_f32_e32 v193, s98, v192
	v_sub_f32_e32 v193, v193, v10
	v_sub_f32_e32 v192, v192, v228
	v_cvt_pk_bf16_f32 v193, v193, v195
	ds_write_b16 v47, v193 offset:2176
	v_lshlrev_b32_e32 v11, 16, v11
	v_add_f32_e32 v192, v192, v11
	v_lshlrev_b32_e32 v229, 16, v229
	v_mul_f32_e32 v193, s98, v192
	v_sub_f32_e32 v193, v193, v11
	v_sub_f32_e32 v192, v192, v229
	v_cvt_pk_bf16_f32 v193, v193, v195
	ds_write_b16 v47, v193 offset:2448
	v_lshlrev_b32_e32 v12, 16, v12
	v_add_f32_e32 v192, v192, v12
	v_lshlrev_b32_e32 v230, 16, v230
	v_mul_f32_e32 v193, s98, v192
	v_sub_f32_e32 v193, v193, v12
	v_sub_f32_e32 v192, v192, v230
	v_cvt_pk_bf16_f32 v193, v193, v195
	ds_write_b16 v47, v193 offset:2720
	v_lshlrev_b32_e32 v13, 16, v13
	v_add_f32_e32 v192, v192, v13
	v_lshlrev_b32_e32 v231, 16, v231
	v_mul_f32_e32 v193, s98, v192
	v_sub_f32_e32 v193, v193, v13
	v_sub_f32_e32 v192, v192, v231
	v_cvt_pk_bf16_f32 v193, v193, v195
	ds_write_b16 v47, v193 offset:2992
	v_lshlrev_b32_e32 v14, 16, v14
	v_add_f32_e32 v192, v192, v14
	v_lshlrev_b32_e32 v232, 16, v232
	v_mul_f32_e32 v193, s98, v192
	v_sub_f32_e32 v193, v193, v14
	v_sub_f32_e32 v192, v192, v232
	v_cvt_pk_bf16_f32 v193, v193, v195
	ds_write_b16 v47, v193 offset:3264
	v_lshlrev_b32_e32 v15, 16, v15
	v_add_f32_e32 v192, v192, v15
	v_lshlrev_b32_e32 v233, 16, v233
	v_mul_f32_e32 v193, s98, v192
	v_sub_f32_e32 v193, v193, v15
	v_sub_f32_e32 v192, v192, v233
	v_cvt_pk_bf16_f32 v193, v193, v195
	ds_write_b16 v47, v193 offset:3536
	v_lshlrev_b32_e32 v16, 16, v16
	v_add_f32_e32 v192, v192, v16
	v_lshlrev_b32_e32 v234, 16, v234
	v_mul_f32_e32 v193, s98, v192
	v_sub_f32_e32 v193, v193, v16
	v_sub_f32_e32 v192, v192, v234
	v_cvt_pk_bf16_f32 v193, v193, v195
	ds_write_b16 v47, v193 offset:3808
	s_branch .Lpool_rows_15
.Lpool_rows_special:
	s_min_u32 s0, 1, s99
	v_cvt_f32_u32_e32 v194, s0
	v_lshlrev_b32_e32 v2, 16, v2
	v_rcp_f32_e32 v1, v194
	v_add_f32_e32 v192, v192, v2
	v_lshlrev_b32_e32 v220, 16, v220
	v_mul_f32_e32 v193, v192, v1
	v_fma_f32 v50, -v194, v193, v192
	v_fmac_f32_e32 v193, v50, v1
	v_sub_f32_e32 v193, v193, v2
	v_sub_f32_e32 v192, v192, v220
	v_cvt_pk_bf16_f32 v193, v193, v195
	ds_write_b16 v47, v193
	s_min_u32 s0, 2, s99
	v_cvt_f32_u32_e32 v194, s0
	v_lshlrev_b32_e32 v3, 16, v3
	v_rcp_f32_e32 v1, v194
	v_add_f32_e32 v192, v192, v3
	v_lshlrev_b32_e32 v221, 16, v221
	v_mul_f32_e32 v193, v192, v1
	v_fma_f32 v50, -v194, v193, v192
	v_fmac_f32_e32 v193, v50, v1
	v_sub_f32_e32 v193, v193, v3
	v_sub_f32_e32 v192, v192, v221
	v_cvt_pk_bf16_f32 v193, v193, v195
	ds_write_b16 v47, v193 offset:272
	s_min_u32 s0, 3, s99
	v_cvt_f32_u32_e32 v194, s0
	v_lshlrev_b32_e32 v4, 16, v4
	v_rcp_f32_e32 v1, v194
	v_add_f32_e32 v192, v192, v4
	v_lshlrev_b32_e32 v222, 16, v222
	v_mul_f32_e32 v193, v192, v1
	v_fma_f32 v50, -v194, v193, v192
	v_fmac_f32_e32 v193, v50, v1
	v_sub_f32_e32 v193, v193, v4
	v_sub_f32_e32 v192, v192, v222
	v_cvt_pk_bf16_f32 v193, v193, v195
	ds_write_b16 v47, v193 offset:544
	s_min_u32 s0, 4, s99
	v_cvt_f32_u32_e32 v194, s0
	v_lshlrev_b32_e32 v5, 16, v5
	v_rcp_f32_e32 v1, v194
	v_add_f32_e32 v192, v192, v5
	v_lshlrev_b32_e32 v223, 16, v223
	v_mul_f32_e32 v193, v192, v1
	v_fma_f32 v50, -v194, v193, v192
	v_fmac_f32_e32 v193, v50, v1
	v_sub_f32_e32 v193, v193, v5
	v_sub_f32_e32 v192, v192, v223
	v_cvt_pk_bf16_f32 v193, v193, v195
	ds_write_b16 v47, v193 offset:816
	s_min_u32 s0, 5, s99
	v_cvt_f32_u32_e32 v194, s0
	v_lshlrev_b32_e32 v6, 16, v6
	v_rcp_f32_e32 v1, v194
	v_add_f32_e32 v192, v192, v6
	v_lshlrev_b32_e32 v224, 16, v224
	v_mul_f32_e32 v193, v192, v1
	v_fma_f32 v50, -v194, v193, v192
	v_fmac_f32_e32 v193, v50, v1
	v_sub_f32_e32 v193, v193, v6
	v_sub_f32_e32 v192, v192, v224
	v_cvt_pk_bf16_f32 v193, v193, v195
	ds_write_b16 v47, v193 offset:1088
	s_min_u32 s0, 6, s99
	v_cvt_f32_u32_e32 v194, s0
	v_lshlrev_b32_e32 v7, 16, v7
	v_rcp_f32_e32 v1, v194
	v_add_f32_e32 v192, v192, v7
	v_lshlrev_b32_e32 v225, 16, v225
	v_mul_f32_e32 v193, v192, v1
	v_fma_f32 v50, -v194, v193, v192
	v_fmac_f32_e32 v193, v50, v1
	v_sub_f32_e32 v193, v193, v7
	v_sub_f32_e32 v192, v192, v225
	v_cvt_pk_bf16_f32 v193, v193, v195
	ds_write_b16 v47, v193 offset:1360
	s_min_u32 s0, 7, s99
	v_cvt_f32_u32_e32 v194, s0
	v_lshlrev_b32_e32 v8, 16, v8
	v_rcp_f32_e32 v1, v194
	v_add_f32_e32 v192, v192, v8
	v_lshlrev_b32_e32 v226, 16, v226
	v_mul_f32_e32 v193, v192, v1
	v_fma_f32 v50, -v194, v193, v192
	v_fmac_f32_e32 v193, v50, v1
	v_sub_f32_e32 v193, v193, v8
	v_sub_f32_e32 v192, v192, v226
	v_cvt_pk_bf16_f32 v193, v193, v195
	ds_write_b16 v47, v193 offset:1632
	s_min_u32 s0, 8, s99
	v_cvt_f32_u32_e32 v194, s0
	v_lshlrev_b32_e32 v9, 16, v9
	v_rcp_f32_e32 v1, v194
	v_add_f32_e32 v192, v192, v9
	v_lshlrev_b32_e32 v227, 16, v227
	v_mul_f32_e32 v193, v192, v1
	v_fma_f32 v50, -v194, v193, v192
	v_fmac_f32_e32 v193, v50, v1
	v_sub_f32_e32 v193, v193, v9
	v_sub_f32_e32 v192, v192, v227
	v_cvt_pk_bf16_f32 v193, v193, v195
	ds_write_b16 v47, v193 offset:1904
	s_min_u32 s0, 9, s99
	v_cvt_f32_u32_e32 v194, s0
	v_lshlrev_b32_e32 v10, 16, v10
	v_rcp_f32_e32 v1, v194
	v_add_f32_e32 v192, v192, v10
	v_lshlrev_b32_e32 v228, 16, v228
	v_mul_f32_e32 v193, v192, v1
	v_fma_f32 v50, -v194, v193, v192
	v_fmac_f32_e32 v193, v50, v1
	v_sub_f32_e32 v193, v193, v10
	v_sub_f32_e32 v192, v192, v228
	v_cvt_pk_bf16_f32 v193, v193, v195
	ds_write_b16 v47, v193 offset:2176
	s_min_u32 s0, 10, s99
	v_cvt_f32_u32_e32 v194, s0
	v_lshlrev_b32_e32 v11, 16, v11
	v_rcp_f32_e32 v1, v194
	v_add_f32_e32 v192, v192, v11
	v_lshlrev_b32_e32 v229, 16, v229
	v_mul_f32_e32 v193, v192, v1
	v_fma_f32 v50, -v194, v193, v192
	v_fmac_f32_e32 v193, v50, v1
	v_sub_f32_e32 v193, v193, v11
	v_sub_f32_e32 v192, v192, v229
	v_cvt_pk_bf16_f32 v193, v193, v195
	ds_write_b16 v47, v193 offset:2448
	s_min_u32 s0, 11, s99
	v_cvt_f32_u32_e32 v194, s0
	v_lshlrev_b32_e32 v12, 16, v12
	v_rcp_f32_e32 v1, v194
	v_add_f32_e32 v192, v192, v12
	v_lshlrev_b32_e32 v230, 16, v230
	v_mul_f32_e32 v193, v192, v1
	v_fma_f32 v50, -v194, v193, v192
	v_fmac_f32_e32 v193, v50, v1
	v_sub_f32_e32 v193, v193, v12
	v_sub_f32_e32 v192, v192, v230
	v_cvt_pk_bf16_f32 v193, v193, v195
	ds_write_b16 v47, v193 offset:2720
	s_min_u32 s0, 12, s99
	v_cvt_f32_u32_e32 v194, s0
	v_lshlrev_b32_e32 v13, 16, v13
	v_rcp_f32_e32 v1, v194
	v_add_f32_e32 v192, v192, v13
	v_lshlrev_b32_e32 v231, 16, v231
	v_mul_f32_e32 v193, v192, v1
	v_fma_f32 v50, -v194, v193, v192
	v_fmac_f32_e32 v193, v50, v1
	v_sub_f32_e32 v193, v193, v13
	v_sub_f32_e32 v192, v192, v231
	v_cvt_pk_bf16_f32 v193, v193, v195
	ds_write_b16 v47, v193 offset:2992
	s_min_u32 s0, 13, s99
	v_cvt_f32_u32_e32 v194, s0
	v_lshlrev_b32_e32 v14, 16, v14
	v_rcp_f32_e32 v1, v194
	v_add_f32_e32 v192, v192, v14
	v_lshlrev_b32_e32 v232, 16, v232
	v_mul_f32_e32 v193, v192, v1
	v_fma_f32 v50, -v194, v193, v192
	v_fmac_f32_e32 v193, v50, v1
	v_sub_f32_e32 v193, v193, v14
	v_sub_f32_e32 v192, v192, v232
	v_cvt_pk_bf16_f32 v193, v193, v195
	ds_write_b16 v47, v193 offset:3264
	s_min_u32 s0, 14, s99
	v_cvt_f32_u32_e32 v194, s0
	v_lshlrev_b32_e32 v15, 16, v15
	v_rcp_f32_e32 v1, v194
	v_add_f32_e32 v192, v192, v15
	v_lshlrev_b32_e32 v233, 16, v233
	v_mul_f32_e32 v193, v192, v1
	v_fma_f32 v50, -v194, v193, v192
	v_fmac_f32_e32 v193, v50, v1
	v_sub_f32_e32 v193, v193, v15
	v_sub_f32_e32 v192, v192, v233
	v_cvt_pk_bf16_f32 v193, v193, v195
	ds_write_b16 v47, v193 offset:3536
	s_min_u32 s0, 15, s99
	v_cvt_f32_u32_e32 v194, s0
	v_lshlrev_b32_e32 v16, 16, v16
	v_rcp_f32_e32 v1, v194
	v_add_f32_e32 v192, v192, v16
	v_lshlrev_b32_e32 v234, 16, v234
	v_mul_f32_e32 v193, v192, v1
	v_fma_f32 v50, -v194, v193, v192
	v_fmac_f32_e32 v193, v50, v1
	v_sub_f32_e32 v193, v193, v16
	v_sub_f32_e32 v192, v192, v234
	v_cvt_pk_bf16_f32 v193, v193, v195
	ds_write_b16 v47, v193 offset:3808
.Lpool_rows_15:
	v_lshlrev_b32_e32 v17, 16, v17
	v_add_f32_e32 v192, v192, v17
	v_lshlrev_b32_e32 v235, 16, v235
	v_mul_f32_e32 v193, s98, v192
	v_sub_f32_e32 v193, v193, v17
	v_sub_f32_e32 v192, v192, v235
	v_cvt_pk_bf16_f32 v193, v193, v195
	ds_write_b16 v47, v193 offset:4080
	s_waitcnt lgkmcnt(0)
	v_lshlrev_b32_e32 v18, 16, v18
	v_add_f32_e32 v192, v192, v18
	v_lshlrev_b32_e32 v236, 16, v236
	v_mul_f32_e32 v193, s98, v192
	v_sub_f32_e32 v193, v193, v18
	v_sub_f32_e32 v192, v192, v236
	v_cvt_pk_bf16_f32 v193, v193, v195
	ds_write_b16 v47, v193 offset:4352
	v_lshlrev_b32_e32 v19, 16, v19
	v_add_f32_e32 v192, v192, v19
	v_lshlrev_b32_e32 v237, 16, v237
	v_mul_f32_e32 v193, s98, v192
	v_sub_f32_e32 v193, v193, v19
	v_sub_f32_e32 v192, v192, v237
	v_cvt_pk_bf16_f32 v193, v193, v195
	ds_write_b16 v47, v193 offset:4624
	v_lshlrev_b32_e32 v20, 16, v20
	v_add_f32_e32 v192, v192, v20
	v_lshlrev_b32_e32 v238, 16, v238
	v_mul_f32_e32 v193, s98, v192
	v_sub_f32_e32 v193, v193, v20
	v_sub_f32_e32 v192, v192, v238
	v_cvt_pk_bf16_f32 v193, v193, v195
	ds_write_b16 v47, v193 offset:4896
	v_lshlrev_b32_e32 v21, 16, v21
	v_add_f32_e32 v192, v192, v21
	v_lshlrev_b32_e32 v239, 16, v239
	v_mul_f32_e32 v193, s98, v192
	v_sub_f32_e32 v193, v193, v21
	v_sub_f32_e32 v192, v192, v239
	v_cvt_pk_bf16_f32 v193, v193, v195
	ds_write_b16 v47, v193 offset:5168
	v_lshlrev_b32_e32 v22, 16, v22
	v_add_f32_e32 v192, v192, v22
	v_lshlrev_b32_e32 v240, 16, v240
	v_mul_f32_e32 v193, s98, v192
	v_sub_f32_e32 v193, v193, v22
	v_sub_f32_e32 v192, v192, v240
	v_cvt_pk_bf16_f32 v193, v193, v195
	ds_write_b16 v47, v193 offset:5440
	v_lshlrev_b32_e32 v23, 16, v23
	v_add_f32_e32 v192, v192, v23
	v_lshlrev_b32_e32 v241, 16, v241
	v_mul_f32_e32 v193, s98, v192
	v_sub_f32_e32 v193, v193, v23
	v_sub_f32_e32 v192, v192, v241
	v_cvt_pk_bf16_f32 v193, v193, v195
	ds_write_b16 v47, v193 offset:5712
	v_lshlrev_b32_e32 v24, 16, v24
	v_add_f32_e32 v192, v192, v24
	v_lshlrev_b32_e32 v242, 16, v242
	v_mul_f32_e32 v193, s98, v192
	v_sub_f32_e32 v193, v193, v24
	v_sub_f32_e32 v192, v192, v242
	v_cvt_pk_bf16_f32 v193, v193, v195
	ds_write_b16 v47, v193 offset:5984
	v_lshlrev_b32_e32 v25, 16, v25
	v_add_f32_e32 v192, v192, v25
	v_lshlrev_b32_e32 v243, 16, v243
	v_mul_f32_e32 v193, s98, v192
	v_sub_f32_e32 v193, v193, v25
	v_sub_f32_e32 v192, v192, v243
	v_cvt_pk_bf16_f32 v193, v193, v195
	ds_write_b16 v47, v193 offset:6256
	v_lshlrev_b32_e32 v26, 16, v26
	v_add_f32_e32 v192, v192, v26
	v_lshlrev_b32_e32 v244, 16, v244
	v_mul_f32_e32 v193, s98, v192
	v_sub_f32_e32 v193, v193, v26
	v_sub_f32_e32 v192, v192, v244
	v_cvt_pk_bf16_f32 v193, v193, v195
	ds_write_b16 v47, v193 offset:6528
	v_lshlrev_b32_e32 v27, 16, v27
	v_add_f32_e32 v192, v192, v27
	v_lshlrev_b32_e32 v245, 16, v245
	v_mul_f32_e32 v193, s98, v192
	v_sub_f32_e32 v193, v193, v27
	v_sub_f32_e32 v192, v192, v245
	v_cvt_pk_bf16_f32 v193, v193, v195
	ds_write_b16 v47, v193 offset:6800
	v_lshlrev_b32_e32 v28, 16, v28
	v_add_f32_e32 v192, v192, v28
	v_lshlrev_b32_e32 v246, 16, v246
	v_mul_f32_e32 v193, s98, v192
	v_sub_f32_e32 v193, v193, v28
	v_sub_f32_e32 v192, v192, v246
	v_cvt_pk_bf16_f32 v193, v193, v195
	ds_write_b16 v47, v193 offset:7072
	v_lshlrev_b32_e32 v29, 16, v29
	v_add_f32_e32 v192, v192, v29
	v_lshlrev_b32_e32 v247, 16, v247
	v_mul_f32_e32 v193, s98, v192
	v_sub_f32_e32 v193, v193, v29
	v_sub_f32_e32 v192, v192, v247
	v_cvt_pk_bf16_f32 v193, v193, v195
	ds_write_b16 v47, v193 offset:7344
	v_lshlrev_b32_e32 v30, 16, v30
	v_add_f32_e32 v192, v192, v30
	v_lshlrev_b32_e32 v248, 16, v248
	v_mul_f32_e32 v193, s98, v192
	v_sub_f32_e32 v193, v193, v30
	v_sub_f32_e32 v192, v192, v248
	v_cvt_pk_bf16_f32 v193, v193, v195
	ds_write_b16 v47, v193 offset:7616
	v_lshlrev_b32_e32 v31, 16, v31
	v_add_f32_e32 v192, v192, v31
	v_lshlrev_b32_e32 v249, 16, v249
	v_mul_f32_e32 v193, s98, v192
	v_sub_f32_e32 v193, v193, v31
	v_sub_f32_e32 v192, v192, v249
	v_cvt_pk_bf16_f32 v193, v193, v195
	ds_write_b16 v47, v193 offset:7888
	v_lshlrev_b32_e32 v32, 16, v32
	v_add_f32_e32 v192, v192, v32
	v_lshlrev_b32_e32 v250, 16, v250
	v_mul_f32_e32 v193, s98, v192
	v_sub_f32_e32 v193, v193, v32
	v_sub_f32_e32 v192, v192, v250
	v_cvt_pk_bf16_f32 v193, v193, v195
	ds_write_b16 v47, v193 offset:8160
	v_lshlrev_b32_e32 v33, 16, v33
	v_add_f32_e32 v192, v192, v33
	v_lshlrev_b32_e32 v251, 16, v251
	v_mul_f32_e32 v193, s98, v192
	v_sub_f32_e32 v193, v193, v33
	v_sub_f32_e32 v192, v192, v251
	v_cvt_pk_bf16_f32 v193, v193, v195
	ds_write_b16 v47, v193 offset:8432
	s_waitcnt lgkmcnt(0)
	s_barrier
	ds_read_b128 v[220:223], v51
	ds_read_b128 v[224:227], v51 offset:32
	ds_read_b128 v[228:231], v51 offset:64
	ds_read_b128 v[232:235], v51 offset:96
	ds_read_b128 v[236:239], v51 offset:128
	ds_read_b128 v[240:243], v51 offset:160
	ds_read_b128 v[244:247], v51 offset:192
	ds_read_b128 v[248:251], v51 offset:224
	s_lshl_b32 s22, s17, 10
	s_lshl_b32 s23, s16, 7
	s_add_i32 s22, s22, s23
	s_add_u32 s18, s40, s22
	s_addc_u32 s19, s41, 0
	s_waitcnt lgkmcnt(7)
	v_mfma_f32_32x32x16_bf16 v[2:17], v[128:131], v[220:223], 0
	v_mfma_f32_32x32x16_bf16 v[18:33], v[160:163], v[220:223], 0
	s_waitcnt lgkmcnt(6)
	v_mfma_f32_32x32x16_bf16 v[2:17], v[132:135], v[224:227], v[2:17]
	v_mfma_f32_32x32x16_bf16 v[18:33], v[164:167], v[224:227], v[18:33]
	s_waitcnt lgkmcnt(5)
	v_mfma_f32_32x32x16_bf16 v[2:17], v[136:139], v[228:231], v[2:17]
	v_mfma_f32_32x32x16_bf16 v[18:33], v[168:171], v[228:231], v[18:33]
	s_waitcnt lgkmcnt(4)
	v_mfma_f32_32x32x16_bf16 v[2:17], v[140:143], v[232:235], v[2:17]
	v_mfma_f32_32x32x16_bf16 v[18:33], v[172:175], v[232:235], v[18:33]
	s_waitcnt lgkmcnt(3)
	v_mfma_f32_32x32x16_bf16 v[2:17], v[144:147], v[236:239], v[2:17]
	v_mfma_f32_32x32x16_bf16 v[18:33], v[176:179], v[236:239], v[18:33]
	s_waitcnt lgkmcnt(2)
	v_mfma_f32_32x32x16_bf16 v[2:17], v[148:151], v[240:243], v[2:17]
	v_mfma_f32_32x32x16_bf16 v[18:33], v[180:183], v[240:243], v[18:33]
	s_waitcnt lgkmcnt(1)
	v_mfma_f32_32x32x16_bf16 v[2:17], v[152:155], v[244:247], v[2:17]
	v_mfma_f32_32x32x16_bf16 v[18:33], v[184:187], v[244:247], v[18:33]
	s_waitcnt lgkmcnt(0)
	v_mfma_f32_32x32x16_bf16 v[2:17], v[156:159], v[248:251], v[2:17]
	v_mfma_f32_32x32x16_bf16 v[18:33], v[188:191], v[248:251], v[18:33]
	s_add_i32 s14, s14, s72
	s_add_i32 s21, s21, 1
	s_nop 7
	s_nop 3
	v_mul_f32_e32 v2, v2, v96
	v_mul_f32_e32 v3, v3, v97
	v_mul_f32_e32 v4, v4, v98
	v_mul_f32_e32 v5, v5, v99
	v_med3_f32 v2, v2, s100, v55
	v_med3_f32 v3, v3, s100, v55
	v_med3_f32 v4, v4, s100, v55
	v_med3_f32 v5, v5, s100, v55
	v_cvt_pk_fp8_f32 v198, v2, v3
	s_nop 0
	v_cvt_pk_fp8_f32 v198, v4, v5 op_sel:[0,0,1]
	v_mul_f32_e32 v6, v6, v100
	v_mul_f32_e32 v7, v7, v101
	v_mul_f32_e32 v8, v8, v102
	v_mul_f32_e32 v9, v9, v103
	v_med3_f32 v6, v6, s100, v55
	v_med3_f32 v7, v7, s100, v55
	v_med3_f32 v8, v8, s100, v55
	v_med3_f32 v9, v9, s100, v55
	v_cvt_pk_fp8_f32 v199, v6, v7
	s_nop 0
	v_cvt_pk_fp8_f32 v199, v8, v9 op_sel:[0,0,1]
	v_mul_f32_e32 v10, v10, v104
	v_mul_f32_e32 v11, v11, v105
	v_mul_f32_e32 v12, v12, v106
	v_mul_f32_e32 v13, v13, v107
	v_med3_f32 v10, v10, s100, v55
	v_med3_f32 v11, v11, s100, v55
	v_med3_f32 v12, v12, s100, v55
	v_med3_f32 v13, v13, s100, v55
	v_cvt_pk_fp8_f32 v200, v10, v11
	s_nop 0
	v_cvt_pk_fp8_f32 v200, v12, v13 op_sel:[0,0,1]
	v_mul_f32_e32 v14, v14, v108
	v_mul_f32_e32 v15, v15, v109
	v_mul_f32_e32 v16, v16, v110
	v_mul_f32_e32 v17, v17, v111
	v_med3_f32 v14, v14, s100, v55
	v_med3_f32 v15, v15, s100, v55
	v_med3_f32 v16, v16, s100, v55
	v_med3_f32 v17, v17, s100, v55
	v_cvt_pk_fp8_f32 v201, v14, v15
	s_nop 0
	v_cvt_pk_fp8_f32 v201, v16, v17 op_sel:[0,0,1]
	v_mul_f32_e32 v18, v18, v112
	v_mul_f32_e32 v19, v19, v113
	v_mul_f32_e32 v20, v20, v114
	v_mul_f32_e32 v21, v21, v115
	v_med3_f32 v18, v18, s100, v55
	v_med3_f32 v19, v19, s100, v55
	v_med3_f32 v20, v20, s100, v55
	v_med3_f32 v21, v21, s100, v55
	v_cvt_pk_fp8_f32 v202, v18, v19
	s_nop 0
	v_cvt_pk_fp8_f32 v202, v20, v21 op_sel:[0,0,1]
	v_mul_f32_e32 v22, v22, v116
	v_mul_f32_e32 v23, v23, v117
	v_mul_f32_e32 v24, v24, v118
	v_mul_f32_e32 v25, v25, v119
	v_med3_f32 v22, v22, s100, v55
	v_med3_f32 v23, v23, s100, v55
	v_med3_f32 v24, v24, s100, v55
	v_med3_f32 v25, v25, s100, v55
	v_cvt_pk_fp8_f32 v203, v22, v23
	s_nop 0
	v_cvt_pk_fp8_f32 v203, v24, v25 op_sel:[0,0,1]
	v_mul_f32_e32 v26, v26, v120
	v_mul_f32_e32 v27, v27, v121
	v_mul_f32_e32 v28, v28, v122
	v_mul_f32_e32 v29, v29, v123
	v_med3_f32 v26, v26, s100, v55
	v_med3_f32 v27, v27, s100, v55
	v_med3_f32 v28, v28, s100, v55
	v_med3_f32 v29, v29, s100, v55
	v_cvt_pk_fp8_f32 v204, v26, v27
	s_nop 0
	v_cvt_pk_fp8_f32 v204, v28, v29 op_sel:[0,0,1]
	v_mul_f32_e32 v30, v30, v124
	v_mul_f32_e32 v31, v31, v125
	v_mul_f32_e32 v32, v32, v126
	v_mul_f32_e32 v33, v33, v127
	v_med3_f32 v30, v30, s100, v55
	v_med3_f32 v31, v31, s100, v55
	v_med3_f32 v32, v32, s100, v55
	v_med3_f32 v33, v33, s100, v55
	v_cvt_pk_fp8_f32 v205, v30, v31
	s_nop 0
	v_cvt_pk_fp8_f32 v205, v32, v33 op_sel:[0,0,1]
	s_nop 1
	v_permlane32_swap_b32_e32 v198, v199
	v_permlane32_swap_b32_e32 v200, v201
	v_permlane32_swap_b32_e32 v202, v203
	v_permlane32_swap_b32_e32 v204, v205
	s_nop 0
	global_store_dwordx2 v54, v[198:199], s[18:19]
	global_store_dwordx2 v54, v[200:201], s[18:19] offset:16
	global_store_dwordx2 v54, v[202:203], s[18:19] offset:32
	global_store_dwordx2 v54, v[204:205], s[18:19] offset:48
	s_cmpk_lt_u32 s14, 0x800
	s_cbranch_scc1 .Lpool_unit
